# scan: swizzle + mid-step second item + incremental addresses for both conversion items + dead SGPR-reload removal
# baseline (speedup 1.0000x reference)
.Lcv1_go:
	v_writelane_b32 v255, s100, 44
	v_writelane_b32 v255, s101, 45
	global_load_dwordx4 v[152:155], v250, s[100:101]
	v_add_u32_e32 v253, 0x2000, v250
	global_load_dwordx4 v[156:159], v253, s[100:101]
	v_add_u32_e32 v252, 0x4000, v250
	global_load_dwordx4 v[160:163], v252, s[100:101]
	v_add_u32_e32 v253, 0x6000, v250
	global_load_dwordx4 v[164:167], v253, s[100:101]
	v_add_u32_e32 v252, 0x8000, v250
	global_load_dwordx4 v[168:171], v252, s[100:101]
	v_add_u32_e32 v253, 0xa000, v250
	global_load_dwordx4 v[172:175], v253, s[100:101]
	v_add_u32_e32 v252, 0xc000, v250
	global_load_dwordx4 v[176:179], v252, s[100:101]
	v_add_u32_e32 v253, 0xe000, v250
	global_load_dwordx4 v[246:249], v253, s[100:101]
	s_lshr_b32 s98, s49, 9
	s_lshl_b32 s98, s98, 8
	s_cmp_lt_u32 s7, 60
	s_cselect_b32 s0, s98, 0
	s_cselect_b32 s1, s7, 0
	s_and_b32 s1, s1, 1
	s_cmp_lg_u32 s1, 0
	s_cselect_b64 s[94:95], -1, 0
	s_add_i32 s0, s0, s44
	s_lshl_b32 s0, s0, 3
	v_readlane_b32 s1, v255, 15
	s_add_i32 s28, s1, s0
	s_bfe_u32 s93, s28, 0x5000b
	s_ashr_i32 s57, s28, 16
	s_lshl_b32 s13, s93, 22
	s_cmp_eq_u32 s57, 3
	s_cselect_b64 s[96:97], -1, 0
	s_cmp_eq_u32 s93, 0
	s_cselect_b64 s[0:1], -1, 0
	s_lshl_b32 s34, s28, 5
	s_and_b32 s37, s34, 0x7e0
	s_and_b32 s36, s28, 0x7c0
	s_mov_b32 s38, s86
	s_and_b32 s98, s7, 1
	s_cmp_gt_u32 s7, 59
	s_cselect_b32 s98, 1, s98
	s_sub_u32 s99, s7, 2
	s_cmp_lt_u32 s99, 53
	s_cselect_b32 s98, 1, s98
	s_cmp_lg_u32 s98, 0
	s_nop 4
	v_readlane_b32 s62, v254, 22
	s_nop 7
	s_cbranch_scc1 .LBB0_424
	v_readlane_b32 s80, v254, 36
	s_cmp_eq_u32 s57, 1
	v_readlane_b32 s81, v254, 37
	v_readlane_b32 s82, v254, 38
	v_readlane_b32 s83, v254, 39
	s_cselect_b32 s29, s80, s82
	s_cselect_b32 s30, s81, s83
	s_nop 0
	s_cmp_lt_u32 s28, 0x10000
	v_readlane_b32 s82, v254, 58
	v_readlane_b32 s83, v254, 59
	s_cselect_b32 s28, s83, s30
	s_cselect_b32 s29, s82, s29
	s_lshl_b32 s30, s13, 2
	s_nop 6
	s_add_u32 s30, s29, s30
	s_addc_u32 s31, s28, 0
	s_nop 0
	v_readlane_b32 s78, v254, 54
	v_readlane_b32 s79, v254, 55
	s_and_b64 s[28:29], s[0:1], exec
	v_readlane_b32 s74, v254, 34
	v_readlane_b32 s75, v254, 35
	s_cselect_b32 s60, s74, s78
	s_cselect_b32 vcc_lo, s75, s79
	s_and_b64 s[28:29], s[96:97], exec
	s_cselect_b32 s29, vcc_lo, s31
	s_cselect_b32 s28, s60, s30
	s_lshl_b32 s98, s36, 13
	s_lshl_b32 s40, s37, 2
	s_add_u32 s98, s98, s40
	s_add_u32 s100, s28, s98
	s_addc_u32 s101, s29, 0
	v_writelane_b32 v255, s100, 48
	v_writelane_b32 v255, s101, 49
	global_load_dwordx4 v[2:5], v250, s[100:101]
	v_add_u32_e32 v253, 0x2000, v250
	global_load_dwordx4 v[6:9], v253, s[100:101]
	v_add_u32_e32 v252, 0x4000, v250
	global_load_dwordx4 v[10:13], v252, s[100:101]
	v_add_u32_e32 v253, 0x6000, v250
	global_load_dwordx4 v[14:17], v253, s[100:101]
	v_add_u32_e32 v252, 0x8000, v250
	global_load_dwordx4 v[18:21], v252, s[100:101]
	v_add_u32_e32 v253, 0xa000, v250
	global_load_dwordx4 v[22:25], v253, s[100:101]
	v_add_u32_e32 v252, 0xc000, v250
	global_load_dwordx4 v[26:29], v252, s[100:101]
	v_add_u32_e32 v253, 0xe000, v250
	global_load_dwordx4 v[116:119], v253, s[100:101]
	s_nop 7
	v_readlane_b32 s62, v254, 22
	s_nop 7

.Lcv1f_go:
	v_writelane_b32 v255, s100, 46
	v_writelane_b32 v255, s101, 47
	s_and_b32 s98, s47, 64
	s_cmp_gt_u32 s47, 0xeff
	s_cselect_b32 s98, 1, s98
	s_cmp_lg_u32 s98, 0
	s_cbranch_scc1 .Lcvw_all
	s_waitcnt vmcnt(9)
	s_branch .Lcvw_done

.Lcvw_done:
	v_cvt_pk_bf16_f32 v152, v152, v156
	v_cvt_pk_bf16_f32 v156, v153, v157
	v_cvt_pk_bf16_f32 v238, v154, v158
	v_cvt_pk_bf16_f32 v242, v155, v159
	v_cvt_pk_bf16_f32 v153, v160, v164
	v_cvt_pk_bf16_f32 v157, v161, v165
	v_cvt_pk_bf16_f32 v239, v162, v166
	v_cvt_pk_bf16_f32 v243, v163, v167
	v_cvt_pk_bf16_f32 v154, v168, v172
	v_cvt_pk_bf16_f32 v158, v169, v173
	v_cvt_pk_bf16_f32 v240, v170, v174
	v_cvt_pk_bf16_f32 v244, v171, v175
	v_cvt_pk_bf16_f32 v155, v176, v246
	v_cvt_pk_bf16_f32 v159, v177, v247
	v_cvt_pk_bf16_f32 v241, v178, v248
	v_cvt_pk_bf16_f32 v245, v179, v249
	global_store_dwordx4 v251, v[152:155], s[100:101]
	global_store_dwordx4 v251, v[156:159], s[100:101] offset:128
	global_store_dwordx4 v251, v[238:241], s[100:101] offset:256
	global_store_dwordx4 v251, v[242:245], s[100:101] offset:384
	s_andn2_b64 vcc, exec, s[94:95]
	s_mov_b32 s86, s38
	s_nop 4
	s_cbranch_vccnz .LBB0_410
	s_sub_u32 s98, s47, 192
	s_cmp_lt_u32 s98, 0xd40
	s_cbranch_scc0 .Lcv2f_slow
	v_readlane_b32 s100, v255, 50
	v_readlane_b32 s101, v255, 51
	s_add_u32 s100, s100, 0x800000
	s_addc_u32 s101, s101, 0
	s_branch .Lcv2f_go
